# NSA tile loop: PV V-fragment LDS reads pipelined 3 ahead of the MFMAs
# baseline (speedup 1.0000x reference)
.LBB0_928:
	v_add3_u32 v103, s27, v241, v242
	v_cvt_pk_bf16_f32 v104, v92, v94
	v_cvt_pk_bf16_f32 v105, v96, v98
	v_cvt_pk_bf16_f32 v106, v99, v100
	v_cvt_pk_bf16_f32 v107, v101, v102
	v_cvt_pk_bf16_f32 v98, v87, v88
	v_cvt_pk_bf16_f32 v99, v89, v90
	v_cvt_pk_bf16_f32 v100, v91, v93
	v_cvt_pk_bf16_f32 v101, v95, v97
	v_cvt_pk_bf16_f32 v92, v76, v78
	v_cvt_pk_bf16_f32 v93, v80, v82
	v_cvt_pk_bf16_f32 v94, v83, v84
	v_cvt_pk_bf16_f32 v95, v85, v86
	v_cvt_pk_bf16_f32 v88, v71, v72
	v_cvt_pk_bf16_f32 v89, v73, v74
	v_cvt_pk_bf16_f32 v90, v75, v77
	v_cvt_pk_bf16_f32 v91, v79, v81
	ds_read_b64_tr_b16 v[72:73], v103 offset:17408
	ds_read_b64_tr_b16 v[74:75], v103 offset:19968
	ds_read_b64_tr_b16 v[76:77], v103 offset:17472
	ds_read_b64_tr_b16 v[78:79], v103 offset:20032
	ds_read_b64_tr_b16 v[80:81], v103 offset:17536
	ds_read_b64_tr_b16 v[82:83], v103 offset:20096
	s_andn2_b64 vcc, exec, s[16:17]
	ds_read_b64_tr_b16 v[84:85], v103 offset:17600
	ds_read_b64_tr_b16 v[86:87], v103 offset:20160
	s_waitcnt lgkmcnt(6)
	v_mfma_f32_32x32x16_bf16 v[52:67], v[72:75], v[104:107], v[52:67]
	ds_read_b64_tr_b16 v[72:73], v103 offset:22528
	ds_read_b64_tr_b16 v[74:75], v103 offset:25088
	s_waitcnt lgkmcnt(6)
	v_mfma_f32_32x32x16_bf16 v[36:51], v[76:79], v[104:107], v[36:51]
	ds_read_b64_tr_b16 v[76:77], v103 offset:22592
	ds_read_b64_tr_b16 v[78:79], v103 offset:25152
	s_waitcnt lgkmcnt(6)
	v_mfma_f32_32x32x16_bf16 v[20:35], v[80:83], v[104:107], v[20:35]
	ds_read_b64_tr_b16 v[80:81], v103 offset:22656
	ds_read_b64_tr_b16 v[82:83], v103 offset:25216
	s_waitcnt lgkmcnt(6)
	v_mfma_f32_32x32x16_bf16 v[4:19], v[84:87], v[104:107], v[4:19]
	ds_read_b64_tr_b16 v[84:85], v103 offset:22720
	ds_read_b64_tr_b16 v[86:87], v103 offset:25280
	s_waitcnt lgkmcnt(6)
	v_mfma_f32_32x32x16_bf16 v[52:67], v[72:75], v[98:101], v[52:67]
	ds_read_b64_tr_b16 v[72:73], v103 offset:27648
	ds_read_b64_tr_b16 v[74:75], v103 offset:30208
	s_waitcnt lgkmcnt(6)
	v_mfma_f32_32x32x16_bf16 v[36:51], v[76:79], v[98:101], v[36:51]
	ds_read_b64_tr_b16 v[76:77], v103 offset:27712
	ds_read_b64_tr_b16 v[78:79], v103 offset:30272
	s_waitcnt lgkmcnt(6)
	v_mfma_f32_32x32x16_bf16 v[20:35], v[80:83], v[98:101], v[20:35]
	ds_read_b64_tr_b16 v[80:81], v103 offset:27776
	ds_read_b64_tr_b16 v[82:83], v103 offset:30336
	s_waitcnt lgkmcnt(6)
	v_mfma_f32_32x32x16_bf16 v[4:19], v[84:87], v[98:101], v[4:19]
	ds_read_b64_tr_b16 v[84:85], v103 offset:27840
	ds_read_b64_tr_b16 v[86:87], v103 offset:30400
	s_waitcnt lgkmcnt(6)
	v_mfma_f32_32x32x16_bf16 v[52:67], v[72:75], v[92:95], v[52:67]
	ds_read_b64_tr_b16 v[72:73], v103 offset:32768
	ds_read_b64_tr_b16 v[74:75], v103 offset:35328
	s_waitcnt lgkmcnt(6)
	v_mfma_f32_32x32x16_bf16 v[36:51], v[76:79], v[92:95], v[36:51]
	ds_read_b64_tr_b16 v[76:77], v103 offset:32832
	ds_read_b64_tr_b16 v[78:79], v103 offset:35392
	s_waitcnt lgkmcnt(6)
	v_mfma_f32_32x32x16_bf16 v[20:35], v[80:83], v[92:95], v[20:35]
	ds_read_b64_tr_b16 v[80:81], v103 offset:32896
	ds_read_b64_tr_b16 v[82:83], v103 offset:35456
	s_waitcnt lgkmcnt(6)
	v_mfma_f32_32x32x16_bf16 v[4:19], v[84:87], v[92:95], v[4:19]
	ds_read_b64_tr_b16 v[84:85], v103 offset:32960
	ds_read_b64_tr_b16 v[86:87], v103 offset:35520
	s_waitcnt lgkmcnt(6)
	v_mfma_f32_32x32x16_bf16 v[52:67], v[72:75], v[88:91], v[52:67]
	s_waitcnt lgkmcnt(4)
	v_mfma_f32_32x32x16_bf16 v[36:51], v[76:79], v[88:91], v[36:51]
	s_waitcnt lgkmcnt(2)
	v_mfma_f32_32x32x16_bf16 v[20:35], v[80:83], v[88:91], v[20:35]
	s_waitcnt lgkmcnt(0)
	v_mfma_f32_32x32x16_bf16 v[4:19], v[84:87], v[88:91], v[4:19]
	s_cbranch_vccnz .LBB0_909
	v_sub_co_u32_e64 v71, s[16:17], s23, 1
	s_nop 0
	v_readfirstlane_b32 s18, v71
	s_xor_b32 s24, s24, 1
	s_and_b32 s23, s18, s23
	s_and_b64 s[16:17], s[16:17], exec
	s_cselect_b32 s16, -1, s26
	s_mov_b32 s22, s25
	s_mov_b32 s25, s16
	v_add_f32_e32 v80, v69, v70
	s_andn2_b64 vcc, exec, s[14:15]
	v_fmac_f32_e32 v80, v247, v68
	s_cbranch_vccnz .LBB0_910
	s_branch .LBB0_905
